# SwiGLU epilogue rewritten by hand: scales folded into the exp2 constant and rcp(128(1+e)), 452 instr instead of 538, f32 math unchanged
# speedup vs baseline: 1.0116x; 1.0116x over previous
.LBB0_1659:
	s_mov_b32 s18, 0xbd38aa3b
	s_mov_b32 s20, 0x43000000
	v_lshl_add_u32 v6, s52, 8, v215
	v_readlane_b32 s4, v246, 11
	v_readlane_b32 s5, v246, 12
	v_ashrrev_i32_e32 v7, 31, v6
	v_lshl_or_b32 v4, s53, 7, v216
	v_lshlrev_b64 v[6:7], 10, v[6:7]
	v_ashrrev_i32_e32 v5, 31, v4
	v_lshl_add_u64 v[6:7], s[4:5], 0, v[6:7]
	v_lshl_add_u64 v[248:249], v[6:7], 0, v[4:5]
	v_mul_f32_e32 v2, s18, v190
	v_mul_f32_e32 v6, s18, v186
	v_mul_f32_e32 v3, s18, v191
	v_mul_f32_e32 v7, s18, v187
	v_mul_f32_e32 v4, s18, v192
	v_mul_f32_e32 v16, s18, v188
	v_mul_f32_e32 v5, s18, v193
	v_mul_f32_e32 v17, s18, v189
	v_exp_f32_e32 v2, v2
	v_exp_f32_e32 v6, v6
	v_exp_f32_e32 v3, v3
	v_exp_f32_e32 v7, v7
	v_exp_f32_e32 v4, v4
	v_exp_f32_e32 v16, v16
	v_exp_f32_e32 v5, v5
	v_exp_f32_e32 v17, v17
	v_pk_mul_f32 v[12:13], v[190:191], v[182:183]
	v_pk_mul_f32 v[14:15], v[192:193], v[184:185]
	v_pk_mul_f32 v[18:19], v[186:187], v[178:179]
	v_pk_mul_f32 v[20:21], v[188:189], v[180:181]
	v_fma_f32 v2, v2, s20, s20
	v_fma_f32 v6, v6, s20, s20
	v_fma_f32 v3, v3, s20, s20
	v_fma_f32 v7, v7, s20, s20
	v_fma_f32 v4, v4, s20, s20
	v_fma_f32 v16, v16, s20, s20
	v_fma_f32 v5, v5, s20, s20
	v_fma_f32 v17, v17, s20, s20
	v_rcp_f32_e32 v2, v2
	v_rcp_f32_e32 v6, v6
	v_rcp_f32_e32 v3, v3
	v_rcp_f32_e32 v7, v7
	v_rcp_f32_e32 v4, v4
	v_rcp_f32_e32 v16, v16
	v_rcp_f32_e32 v5, v5
	v_rcp_f32_e32 v17, v17
	v_pk_mul_f32 v[12:13], v[12:13], v[2:3]
	v_pk_mul_f32 v[18:19], v[18:19], v[6:7]
	v_pk_mul_f32 v[14:15], v[14:15], v[4:5]
	v_pk_mul_f32 v[20:21], v[20:21], v[16:17]
	v_med3_f32 v12, v12, s46, v204
	v_med3_f32 v18, v18, s46, v204
	v_med3_f32 v13, v13, s46, v204
	v_med3_f32 v19, v19, s46, v204
	v_med3_f32 v14, v14, s46, v204
	v_med3_f32 v20, v20, s46, v204
	v_med3_f32 v15, v15, s46, v204
	v_med3_f32 v21, v21, s46, v204
	v_cvt_pk_fp8_f32 v8, v12, v13
	v_cvt_pk_fp8_f32 v9, v18, v19
	v_cvt_pk_fp8_f32 v8, v14, v15 op_sel:[0,0,1]
	v_cvt_pk_fp8_f32 v9, v20, v21 op_sel:[0,0,1]
	v_mul_f32_e32 v2, s18, v174
	v_mul_f32_e32 v6, s18, v170
	v_mul_f32_e32 v3, s18, v175
	v_mul_f32_e32 v7, s18, v171
	v_mul_f32_e32 v4, s18, v176
	v_mul_f32_e32 v16, s18, v172
	v_mul_f32_e32 v5, s18, v177
	v_mul_f32_e32 v17, s18, v173
	v_exp_f32_e32 v2, v2
	v_exp_f32_e32 v6, v6
	v_exp_f32_e32 v3, v3
	v_exp_f32_e32 v7, v7
	v_exp_f32_e32 v4, v4
	v_exp_f32_e32 v16, v16
	v_exp_f32_e32 v5, v5
	v_exp_f32_e32 v17, v17
	v_pk_mul_f32 v[12:13], v[174:175], v[166:167]
	v_pk_mul_f32 v[14:15], v[176:177], v[168:169]
	v_pk_mul_f32 v[18:19], v[170:171], v[162:163]
	v_pk_mul_f32 v[20:21], v[172:173], v[164:165]
	v_fma_f32 v2, v2, s20, s20
	v_fma_f32 v6, v6, s20, s20
	v_fma_f32 v3, v3, s20, s20
	v_fma_f32 v7, v7, s20, s20
	v_fma_f32 v4, v4, s20, s20
	v_fma_f32 v16, v16, s20, s20
	v_fma_f32 v5, v5, s20, s20
	v_fma_f32 v17, v17, s20, s20
	v_rcp_f32_e32 v2, v2
	v_rcp_f32_e32 v6, v6
	v_rcp_f32_e32 v3, v3
	v_rcp_f32_e32 v7, v7
	v_rcp_f32_e32 v4, v4
	v_rcp_f32_e32 v16, v16
	v_rcp_f32_e32 v5, v5
	v_rcp_f32_e32 v17, v17
	v_pk_mul_f32 v[12:13], v[12:13], v[2:3]
	v_pk_mul_f32 v[18:19], v[18:19], v[6:7]
	v_pk_mul_f32 v[14:15], v[14:15], v[4:5]
	v_pk_mul_f32 v[20:21], v[20:21], v[16:17]
	v_med3_f32 v12, v12, s46, v204
	v_med3_f32 v18, v18, s46, v204
	v_med3_f32 v13, v13, s46, v204
	v_med3_f32 v19, v19, s46, v204
	v_med3_f32 v14, v14, s46, v204
	v_med3_f32 v20, v20, s46, v204
	v_med3_f32 v15, v15, s46, v204
	v_med3_f32 v21, v21, s46, v204
	v_cvt_pk_fp8_f32 v10, v12, v13
	v_cvt_pk_fp8_f32 v11, v18, v19
	v_cvt_pk_fp8_f32 v10, v14, v15 op_sel:[0,0,1]
	v_cvt_pk_fp8_f32 v11, v20, v21 op_sel:[0,0,1]
	v_mov_b32_e32 v250, v248
	v_mov_b32_e32 v251, v249
	v_permlane16_swap_b32_e32 v8, v10
	v_permlane16_swap_b32_e32 v9, v11
	global_store_dwordx4 v[250:251], v[8:11], off
	v_mul_f32_e32 v2, s18, v158
	v_mul_f32_e32 v6, s18, v154
	v_mul_f32_e32 v3, s18, v159
	v_mul_f32_e32 v7, s18, v155
	v_mul_f32_e32 v4, s18, v160
	v_mul_f32_e32 v16, s18, v156
	v_mul_f32_e32 v5, s18, v161
	v_mul_f32_e32 v17, s18, v157
	v_exp_f32_e32 v2, v2
	v_exp_f32_e32 v6, v6
	v_exp_f32_e32 v3, v3
	v_exp_f32_e32 v7, v7
	v_exp_f32_e32 v4, v4
	v_exp_f32_e32 v16, v16
	v_exp_f32_e32 v5, v5
	v_exp_f32_e32 v17, v17
	v_pk_mul_f32 v[12:13], v[158:159], v[150:151]
	v_pk_mul_f32 v[14:15], v[160:161], v[152:153]
	v_pk_mul_f32 v[18:19], v[154:155], v[146:147]
	v_pk_mul_f32 v[20:21], v[156:157], v[148:149]
	v_fma_f32 v2, v2, s20, s20
	v_fma_f32 v6, v6, s20, s20
	v_fma_f32 v3, v3, s20, s20
	v_fma_f32 v7, v7, s20, s20
	v_fma_f32 v4, v4, s20, s20
	v_fma_f32 v16, v16, s20, s20
	v_fma_f32 v5, v5, s20, s20
	v_fma_f32 v17, v17, s20, s20
	v_rcp_f32_e32 v2, v2
	v_rcp_f32_e32 v6, v6
	v_rcp_f32_e32 v3, v3
	v_rcp_f32_e32 v7, v7
	v_rcp_f32_e32 v4, v4
	v_rcp_f32_e32 v16, v16
	v_rcp_f32_e32 v5, v5
	v_rcp_f32_e32 v17, v17
	v_pk_mul_f32 v[12:13], v[12:13], v[2:3]
	v_pk_mul_f32 v[18:19], v[18:19], v[6:7]
	v_pk_mul_f32 v[14:15], v[14:15], v[4:5]
	v_pk_mul_f32 v[20:21], v[20:21], v[16:17]
	v_med3_f32 v12, v12, s46, v204
	v_med3_f32 v18, v18, s46, v204
	v_med3_f32 v13, v13, s46, v204
	v_med3_f32 v19, v19, s46, v204
	v_med3_f32 v14, v14, s46, v204
	v_med3_f32 v20, v20, s46, v204
	v_med3_f32 v15, v15, s46, v204
	v_med3_f32 v21, v21, s46, v204
	v_cvt_pk_fp8_f32 v8, v12, v13
	v_cvt_pk_fp8_f32 v9, v18, v19
	v_cvt_pk_fp8_f32 v8, v14, v15 op_sel:[0,0,1]
	v_cvt_pk_fp8_f32 v9, v20, v21 op_sel:[0,0,1]
	v_mul_f32_e32 v2, s18, v142
	v_mul_f32_e32 v6, s18, v138
	v_mul_f32_e32 v3, s18, v143
	v_mul_f32_e32 v7, s18, v139
	v_mul_f32_e32 v4, s18, v144
	v_mul_f32_e32 v16, s18, v140
	v_mul_f32_e32 v5, s18, v145
	v_mul_f32_e32 v17, s18, v141
	v_exp_f32_e32 v2, v2
	v_exp_f32_e32 v6, v6
	v_exp_f32_e32 v3, v3
	v_exp_f32_e32 v7, v7
	v_exp_f32_e32 v4, v4
	v_exp_f32_e32 v16, v16
	v_exp_f32_e32 v5, v5
	v_exp_f32_e32 v17, v17
	v_pk_mul_f32 v[12:13], v[142:143], v[134:135]
	v_pk_mul_f32 v[14:15], v[144:145], v[136:137]
	v_pk_mul_f32 v[18:19], v[138:139], v[130:131]
	v_pk_mul_f32 v[20:21], v[140:141], v[132:133]
	v_fma_f32 v2, v2, s20, s20
	v_fma_f32 v6, v6, s20, s20
	v_fma_f32 v3, v3, s20, s20
	v_fma_f32 v7, v7, s20, s20
	v_fma_f32 v4, v4, s20, s20
	v_fma_f32 v16, v16, s20, s20
	v_fma_f32 v5, v5, s20, s20
	v_fma_f32 v17, v17, s20, s20
	v_rcp_f32_e32 v2, v2
	v_rcp_f32_e32 v6, v6
	v_rcp_f32_e32 v3, v3
	v_rcp_f32_e32 v7, v7
	v_rcp_f32_e32 v4, v4
	v_rcp_f32_e32 v16, v16
	v_rcp_f32_e32 v5, v5
	v_rcp_f32_e32 v17, v17
	v_pk_mul_f32 v[12:13], v[12:13], v[2:3]
	v_pk_mul_f32 v[18:19], v[18:19], v[6:7]
	v_pk_mul_f32 v[14:15], v[14:15], v[4:5]
	v_pk_mul_f32 v[20:21], v[20:21], v[16:17]
	v_med3_f32 v12, v12, s46, v204
	v_med3_f32 v18, v18, s46, v204
	v_med3_f32 v13, v13, s46, v204
	v_med3_f32 v19, v19, s46, v204
	v_med3_f32 v14, v14, s46, v204
	v_med3_f32 v20, v20, s46, v204
	v_med3_f32 v15, v15, s46, v204
	v_med3_f32 v21, v21, s46, v204
	v_cvt_pk_fp8_f32 v10, v12, v13
	v_cvt_pk_fp8_f32 v11, v18, v19
	v_cvt_pk_fp8_f32 v10, v14, v15 op_sel:[0,0,1]
	v_cvt_pk_fp8_f32 v11, v20, v21 op_sel:[0,0,1]
	s_mov_b64 s[4:5], 0x8000
	v_lshl_add_u64 v[250:251], v[248:249], 0, s[4:5]
	s_nop 0
	v_permlane16_swap_b32_e32 v8, v10
	v_permlane16_swap_b32_e32 v9, v11
	global_store_dwordx4 v[250:251], v[8:11], off
	v_mul_f32_e32 v2, s18, v126
	v_mul_f32_e32 v6, s18, v122
	v_mul_f32_e32 v3, s18, v127
	v_mul_f32_e32 v7, s18, v123
	v_mul_f32_e32 v4, s18, v128
	v_mul_f32_e32 v16, s18, v124
	v_mul_f32_e32 v5, s18, v129
	v_mul_f32_e32 v17, s18, v125
	v_exp_f32_e32 v2, v2
	v_exp_f32_e32 v6, v6
	v_exp_f32_e32 v3, v3
	v_exp_f32_e32 v7, v7
	v_exp_f32_e32 v4, v4
	v_exp_f32_e32 v16, v16
	v_exp_f32_e32 v5, v5
	v_exp_f32_e32 v17, v17
	v_pk_mul_f32 v[12:13], v[126:127], v[118:119]
	v_pk_mul_f32 v[14:15], v[128:129], v[120:121]
	v_pk_mul_f32 v[18:19], v[122:123], v[114:115]
	v_pk_mul_f32 v[20:21], v[124:125], v[116:117]
	v_fma_f32 v2, v2, s20, s20
	v_fma_f32 v6, v6, s20, s20
	v_fma_f32 v3, v3, s20, s20
	v_fma_f32 v7, v7, s20, s20
	v_fma_f32 v4, v4, s20, s20
	v_fma_f32 v16, v16, s20, s20
	v_fma_f32 v5, v5, s20, s20
	v_fma_f32 v17, v17, s20, s20
	v_rcp_f32_e32 v2, v2
	v_rcp_f32_e32 v6, v6
	v_rcp_f32_e32 v3, v3
	v_rcp_f32_e32 v7, v7
	v_rcp_f32_e32 v4, v4
	v_rcp_f32_e32 v16, v16
	v_rcp_f32_e32 v5, v5
	v_rcp_f32_e32 v17, v17
	v_pk_mul_f32 v[12:13], v[12:13], v[2:3]
	v_pk_mul_f32 v[18:19], v[18:19], v[6:7]
	v_pk_mul_f32 v[14:15], v[14:15], v[4:5]
	v_pk_mul_f32 v[20:21], v[20:21], v[16:17]
	v_med3_f32 v12, v12, s46, v204
	v_med3_f32 v18, v18, s46, v204
	v_med3_f32 v13, v13, s46, v204
	v_med3_f32 v19, v19, s46, v204
	v_med3_f32 v14, v14, s46, v204
	v_med3_f32 v20, v20, s46, v204
	v_med3_f32 v15, v15, s46, v204
	v_med3_f32 v21, v21, s46, v204
	v_cvt_pk_fp8_f32 v8, v12, v13
	v_cvt_pk_fp8_f32 v9, v18, v19
	v_cvt_pk_fp8_f32 v8, v14, v15 op_sel:[0,0,1]
	v_cvt_pk_fp8_f32 v9, v20, v21 op_sel:[0,0,1]
	v_mul_f32_e32 v2, s18, v110
	v_mul_f32_e32 v6, s18, v106
	v_mul_f32_e32 v3, s18, v111
	v_mul_f32_e32 v7, s18, v107
	v_mul_f32_e32 v4, s18, v112
	v_mul_f32_e32 v16, s18, v108
	v_mul_f32_e32 v5, s18, v113
	v_mul_f32_e32 v17, s18, v109
	v_exp_f32_e32 v2, v2
	v_exp_f32_e32 v6, v6
	v_exp_f32_e32 v3, v3
	v_exp_f32_e32 v7, v7
	v_exp_f32_e32 v4, v4
	v_exp_f32_e32 v16, v16
	v_exp_f32_e32 v5, v5
	v_exp_f32_e32 v17, v17
	v_pk_mul_f32 v[12:13], v[110:111], v[102:103]
	v_pk_mul_f32 v[14:15], v[112:113], v[104:105]
	v_pk_mul_f32 v[18:19], v[106:107], v[90:91]
	v_pk_mul_f32 v[20:21], v[108:109], v[92:93]
	v_fma_f32 v2, v2, s20, s20
	v_fma_f32 v6, v6, s20, s20
	v_fma_f32 v3, v3, s20, s20
	v_fma_f32 v7, v7, s20, s20
	v_fma_f32 v4, v4, s20, s20
	v_fma_f32 v16, v16, s20, s20
	v_fma_f32 v5, v5, s20, s20
	v_fma_f32 v17, v17, s20, s20
	v_rcp_f32_e32 v2, v2
	v_rcp_f32_e32 v6, v6
	v_rcp_f32_e32 v3, v3
	v_rcp_f32_e32 v7, v7
	v_rcp_f32_e32 v4, v4
	v_rcp_f32_e32 v16, v16
	v_rcp_f32_e32 v5, v5
	v_rcp_f32_e32 v17, v17
	v_pk_mul_f32 v[12:13], v[12:13], v[2:3]
	v_pk_mul_f32 v[18:19], v[18:19], v[6:7]
	v_pk_mul_f32 v[14:15], v[14:15], v[4:5]
	v_pk_mul_f32 v[20:21], v[20:21], v[16:17]
	v_med3_f32 v12, v12, s46, v204
	v_med3_f32 v18, v18, s46, v204
	v_med3_f32 v13, v13, s46, v204
	v_med3_f32 v19, v19, s46, v204
	v_med3_f32 v14, v14, s46, v204
	v_med3_f32 v20, v20, s46, v204
	v_med3_f32 v15, v15, s46, v204
	v_med3_f32 v21, v21, s46, v204
	v_cvt_pk_fp8_f32 v10, v12, v13
	v_cvt_pk_fp8_f32 v11, v18, v19
	v_cvt_pk_fp8_f32 v10, v14, v15 op_sel:[0,0,1]
	v_cvt_pk_fp8_f32 v11, v20, v21 op_sel:[0,0,1]
	s_mov_b64 s[4:5], 0x20000
	v_lshl_add_u64 v[250:251], v[248:249], 0, s[4:5]
	s_nop 0
	v_permlane16_swap_b32_e32 v8, v10
	v_permlane16_swap_b32_e32 v9, v11
	global_store_dwordx4 v[250:251], v[8:11], off
	v_mul_f32_e32 v2, s18, v86
	v_mul_f32_e32 v6, s18, v82
	v_mul_f32_e32 v3, s18, v87
	v_mul_f32_e32 v7, s18, v83
	v_mul_f32_e32 v4, s18, v88
	v_mul_f32_e32 v16, s18, v84
	v_mul_f32_e32 v5, s18, v89
	v_mul_f32_e32 v17, s18, v85
	v_exp_f32_e32 v2, v2
	v_exp_f32_e32 v6, v6
	v_exp_f32_e32 v3, v3
	v_exp_f32_e32 v7, v7
	v_exp_f32_e32 v4, v4
	v_exp_f32_e32 v16, v16
	v_exp_f32_e32 v5, v5
	v_exp_f32_e32 v17, v17
	v_pk_mul_f32 v[12:13], v[86:87], v[98:99]
	v_pk_mul_f32 v[14:15], v[88:89], v[100:101]
	v_pk_mul_f32 v[18:19], v[82:83], v[94:95]
	v_pk_mul_f32 v[20:21], v[84:85], v[96:97]
	v_fma_f32 v2, v2, s20, s20
	v_fma_f32 v6, v6, s20, s20
	v_fma_f32 v3, v3, s20, s20
	v_fma_f32 v7, v7, s20, s20
	v_fma_f32 v4, v4, s20, s20
	v_fma_f32 v16, v16, s20, s20
	v_fma_f32 v5, v5, s20, s20
	v_fma_f32 v17, v17, s20, s20
	v_rcp_f32_e32 v2, v2
	v_rcp_f32_e32 v6, v6
	v_rcp_f32_e32 v3, v3
	v_rcp_f32_e32 v7, v7
	v_rcp_f32_e32 v4, v4
	v_rcp_f32_e32 v16, v16
	v_rcp_f32_e32 v5, v5
	v_rcp_f32_e32 v17, v17
	v_pk_mul_f32 v[12:13], v[12:13], v[2:3]
	v_pk_mul_f32 v[18:19], v[18:19], v[6:7]
	v_pk_mul_f32 v[14:15], v[14:15], v[4:5]
	v_pk_mul_f32 v[20:21], v[20:21], v[16:17]
	v_med3_f32 v12, v12, s46, v204
	v_med3_f32 v18, v18, s46, v204
	v_med3_f32 v13, v13, s46, v204
	v_med3_f32 v19, v19, s46, v204
	v_med3_f32 v14, v14, s46, v204
	v_med3_f32 v20, v20, s46, v204
	v_med3_f32 v15, v15, s46, v204
	v_med3_f32 v21, v21, s46, v204
	v_cvt_pk_fp8_f32 v8, v12, v13
	v_cvt_pk_fp8_f32 v9, v18, v19
	v_cvt_pk_fp8_f32 v8, v14, v15 op_sel:[0,0,1]
	v_cvt_pk_fp8_f32 v9, v20, v21 op_sel:[0,0,1]
	v_mul_f32_e32 v2, s18, v70
	v_mul_f32_e32 v6, s18, v66
	v_mul_f32_e32 v3, s18, v71
	v_mul_f32_e32 v7, s18, v67
	v_mul_f32_e32 v4, s18, v72
	v_mul_f32_e32 v16, s18, v68
	v_mul_f32_e32 v5, s18, v73
	v_mul_f32_e32 v17, s18, v69
	v_exp_f32_e32 v2, v2
	v_exp_f32_e32 v6, v6
	v_exp_f32_e32 v3, v3
	v_exp_f32_e32 v7, v7
	v_exp_f32_e32 v4, v4
	v_exp_f32_e32 v16, v16
	v_exp_f32_e32 v5, v5
	v_exp_f32_e32 v17, v17
	v_pk_mul_f32 v[12:13], v[70:71], v[78:79]
	v_pk_mul_f32 v[14:15], v[72:73], v[80:81]
	v_pk_mul_f32 v[18:19], v[66:67], v[74:75]
	v_pk_mul_f32 v[20:21], v[68:69], v[76:77]
	v_fma_f32 v2, v2, s20, s20
	v_fma_f32 v6, v6, s20, s20
	v_fma_f32 v3, v3, s20, s20
	v_fma_f32 v7, v7, s20, s20
	v_fma_f32 v4, v4, s20, s20
	v_fma_f32 v16, v16, s20, s20
	v_fma_f32 v5, v5, s20, s20
	v_fma_f32 v17, v17, s20, s20
	v_rcp_f32_e32 v2, v2
	v_rcp_f32_e32 v6, v6
	v_rcp_f32_e32 v3, v3
	v_rcp_f32_e32 v7, v7
	v_rcp_f32_e32 v4, v4
	v_rcp_f32_e32 v16, v16
	v_rcp_f32_e32 v5, v5
	v_rcp_f32_e32 v17, v17
	v_pk_mul_f32 v[12:13], v[12:13], v[2:3]
	v_pk_mul_f32 v[18:19], v[18:19], v[6:7]
	v_pk_mul_f32 v[14:15], v[14:15], v[4:5]
	v_pk_mul_f32 v[20:21], v[20:21], v[16:17]
	v_med3_f32 v12, v12, s46, v204
	v_med3_f32 v18, v18, s46, v204
	v_med3_f32 v13, v13, s46, v204
	v_med3_f32 v19, v19, s46, v204
	v_med3_f32 v14, v14, s46, v204
	v_med3_f32 v20, v20, s46, v204
	v_med3_f32 v15, v15, s46, v204
	v_med3_f32 v21, v21, s46, v204
	v_cvt_pk_fp8_f32 v10, v12, v13
	v_cvt_pk_fp8_f32 v11, v18, v19
	v_cvt_pk_fp8_f32 v10, v14, v15 op_sel:[0,0,1]
	v_cvt_pk_fp8_f32 v11, v20, v21 op_sel:[0,0,1]
	s_mov_b64 s[4:5], 0x28000
	v_lshl_add_u64 v[250:251], v[248:249], 0, s[4:5]
	s_nop 0
	v_permlane16_swap_b32_e32 v8, v10
	v_permlane16_swap_b32_e32 v9, v11
	s_and_b64 vcc, exec, s[0:1]
	s_mov_b64 s[0:1], -1
	global_store_dwordx4 v[250:251], v[8:11], off
	s_cbranch_vccnz .LBB0_1638
	s_andn2_b64 vcc, exec, s[8:9]
	s_cbranch_vccnz .LBB0_1637
	s_barrier
	s_branch .LBB0_1637

	.amdhsa_kernel _Z4mega1Pii
		.amdhsa_group_segment_fixed_size 0
		.amdhsa_private_segment_fixed_size 0
		.amdhsa_kernarg_size 480
		.amdhsa_user_sgpr_count 2
		.amdhsa_user_sgpr_dispatch_ptr 0
		.amdhsa_user_sgpr_queue_ptr 0
		.amdhsa_user_sgpr_kernarg_segment_ptr 1
		.amdhsa_user_sgpr_dispatch_id 0
		.amdhsa_user_sgpr_kernarg_preload_length 0
		.amdhsa_user_sgpr_kernarg_preload_offset 0
		.amdhsa_user_sgpr_private_segment_size 0
		.amdhsa_uses_dynamic_stack 0
		.amdhsa_enable_private_segment 0
		.amdhsa_system_sgpr_workgroup_id_x 1
		.amdhsa_system_sgpr_workgroup_id_y 0
		.amdhsa_system_sgpr_workgroup_id_z 0
		.amdhsa_system_sgpr_workgroup_info 0
		.amdhsa_system_vgpr_workitem_id 0
		.amdhsa_next_free_vgpr 252
		.amdhsa_next_free_sgpr 100
		.amdhsa_accum_offset 252
		.amdhsa_reserve_vcc 1
		.amdhsa_float_round_mode_32 0
		.amdhsa_float_round_mode_16_64 0
		.amdhsa_float_denorm_mode_32 3
		.amdhsa_float_denorm_mode_16_64 3
		.amdhsa_dx10_clamp 1
		.amdhsa_ieee_mode 1
		.amdhsa_fp16_overflow 0
		.amdhsa_tg_split 0
		.amdhsa_exception_fp_ieee_invalid_op 0
		.amdhsa_exception_fp_denorm_src 0
		.amdhsa_exception_fp_ieee_div_zero 0
		.amdhsa_exception_fp_ieee_overflow 0
		.amdhsa_exception_fp_ieee_underflow 0
		.amdhsa_exception_fp_ieee_inexact 0
		.amdhsa_exception_int_div_zero 0
	.end_amdhsa_kernel

amdhsa.kernels:
  - .agpr_count:     0
    .args:
      - .offset:         0
        .size:           216
        .value_kind:     by_value
      - .offset:         216
        .size:           4
        .value_kind:     by_value
      - .offset:         220
        .size:           4
        .value_kind:     by_value
      - .offset:         224
        .size:           4
        .value_kind:     hidden_block_count_x
      - .offset:         228
        .size:           4
        .value_kind:     hidden_block_count_y
      - .offset:         232
        .size:           4
        .value_kind:     hidden_block_count_z
      - .offset:         236
        .size:           2
        .value_kind:     hidden_group_size_x
      - .offset:         238
        .size:           2
        .value_kind:     hidden_group_size_y
      - .offset:         240
        .size:           2
        .value_kind:     hidden_group_size_z
      - .offset:         242
        .size:           2
        .value_kind:     hidden_remainder_x
      - .offset:         244
        .size:           2
        .value_kind:     hidden_remainder_y
      - .offset:         246
        .size:           2
        .value_kind:     hidden_remainder_z
      - .offset:         264
        .size:           8
        .value_kind:     hidden_global_offset_x
      - .offset:         272
        .size:           8
        .value_kind:     hidden_global_offset_y
      - .offset:         280
        .size:           8
        .value_kind:     hidden_global_offset_z
      - .offset:         288
        .size:           2
        .value_kind:     hidden_grid_dims
      - .offset:         344
        .size:           4
        .value_kind:     hidden_dynamic_lds_size
    .group_segment_fixed_size: 0
    .kernarg_segment_align: 8
    .kernarg_segment_size: 480
    .language:       OpenCL C
    .language_version:
      - 2
      - 0
    .max_flat_workgroup_size: 512
    .name:           _Z4mega1Pii
    .private_segment_fixed_size: 0
    .sgpr_count:     106
    .sgpr_spill_count: 438
    .symbol:         _Z4mega1Pii.kd
    .uniform_work_group_size: 1
    .uses_dynamic_stack: false
    .vgpr_count:     252
    .vgpr_spill_count: 0
    .wavefront_size: 64
